# one static s_setprio 1 for waves 0-3 around the NSA tile loops (reset at loop exit)
# speedup vs baseline: 1.0060x; 1.0060x over previous
; __device__ __forceinline__ void nsa_unit(const Args& a, LAS unsigned char* lds, int b, int kvh, int qb) {
;     ...
;     float mrun = -1e30f, lrun = 0.f;
;     f32x16 p0, p1;
; #pragma unroll
;     for (int i = 0; i < 16; ++i) { p0[i] = 0.f; p1[i] = 0.f; }
;     bf16x8 pf[2][2];
;     if (w >= 4) asm volatile("s_barrier" ::: "memory");
; #pragma unroll 1
;     for (int it = 0; it <= nTot; ++it) {
.Lcn_lgo_n0s:
	v_and_b32_e32 v224, 63, v0
	v_and_b32_e32 v253, 7, v224
	v_lshrrev_b32_e32 v224, 3, v224
	v_lshlrev_b32_e32 v224, 2, v224
	v_lshlrev_b32_e32 v225, 4, v253
	v_lshlrev_b32_e32 v253, 2, v253
	v_mad_u32_u24 v254, v224, s65, v225
	global_load_dwordx4 v[212:215], v254, s[32:33] nt
	s_add_u32 s32, s32, s65
	s_addc_u32 s33, s33, 0
	global_load_dwordx4 v[216:219], v254, s[32:33] nt
	s_add_u32 s32, s32, s65
	s_addc_u32 s33, s33, 0
	global_load_dwordx4 v[220:223], v254, s[32:33] nt
	s_add_u32 s32, s32, s65
	s_addc_u32 s33, s33, 0
	global_load_dwordx2 v[224:225], v254, s[32:33] offset:0 nt
	global_load_dword v253, v254, s[32:33] offset:8 nt
	global_load_dword v254, v254, s[32:33] offset:12 nt
	v_readfirstlane_b32 s12, v0
	s_nop 3
	s_lshr_b32 s12, s12, 6
	s_cmp_ge_u32 s12, 4
	s_cbranch_scc1 .Lprio_done_n0
	s_setprio 1

; __device__ __forceinline__ void nsa_unit(const Args& a, LAS unsigned char* lds, int b, int kvh, int qb) {
;     ...
;     float mrun = -1e30f, lrun = 0.f;
;     f32x16 p0, p1;
; #pragma unroll
;     for (int i = 0; i < 16; ++i) { p0[i] = 0.f; p1[i] = 0.f; }
;     bf16x8 pf[2][2];
;     if (w >= 4) asm volatile("s_barrier" ::: "memory");
; #pragma unroll 1
;     for (int it = 0; it <= nTot; ++it) {
.Lcn_lgo_n1s:
	v_and_b32_e32 v220, 63, v0
	v_and_b32_e32 v253, 7, v220
	v_lshrrev_b32_e32 v220, 3, v220
	v_lshlrev_b32_e32 v220, 2, v220
	v_lshlrev_b32_e32 v221, 4, v253
	v_lshlrev_b32_e32 v253, 2, v253
	v_mad_u32_u24 v254, v220, vcc_lo, v221
	global_load_dwordx4 v[212:215], v254, s[32:33] nt
	s_add_u32 s32, s32, vcc_lo
	s_addc_u32 s33, s33, 0
	global_load_dwordx4 v[216:219], v254, s[32:33] nt
	s_add_u32 s32, s32, vcc_lo
	s_addc_u32 s33, s33, 0
	global_load_dwordx4 v[224:227], v254, s[32:33] nt
	s_add_u32 s32, s32, vcc_lo
	s_addc_u32 s33, s33, 0
	global_load_dwordx2 v[220:221], v254, s[32:33] offset:0 nt
	global_load_dword v253, v254, s[32:33] offset:8 nt
	global_load_dword v254, v254, s[32:33] offset:12 nt
	v_readfirstlane_b32 s14, v0
	s_nop 3
	s_lshr_b32 s14, s14, 6
	s_cmp_ge_u32 s14, 4
	s_cbranch_scc1 .Lprio_done_n1
	s_setprio 1
